# speedup vs baseline: 1.0159x; 1.0096x over previous
_Z8dog_mainPKfS0_S0_S0_S0_S0_S0_Pf:
	s_load_dwordx8 s[12:19], s[0:1], 0x0
	s_load_dwordx8 s[20:27], s[0:1], 0x20
	s_and_b32 s3, s2, 7
	s_lshl_b32 s3, s3, 5
	s_lshr_b32 s4, s2, 3
	s_add_i32 s4, s3, s4
	s_and_b32 s6, s4, 3
	s_lshr_b32 s7, s4, 2
	s_mov_b32 s5, 0
	s_lshl_b64 s[8:9], s[4:5], 18
	v_and_b32_e32 v1, 63, v0
	v_lshrrev_b32_e32 v2, 6, v0
	v_and_b32_e32 v3, 31, v0
	v_lshl_or_b32 v4, v2, 5, v3
	v_lshlrev_b32_e32 v5, 2, v4
	v_lshlrev_b32_e32 v6, 4, v1
	v_lshl_or_b32 v6, v2, 15, v6
	v_bfe_u32 v7, v0, 5, 1
	s_waitcnt lgkmcnt(0)
	global_load_dword v20, v5, s[18:19]
	global_load_dword v21, v5, s[20:21]
	global_load_dword v22, v5, s[22:23]
	global_load_dword v23, v5, s[24:25]
	global_load_dword v24, v5, s[14:15]
	global_load_dword v25, v5, s[16:17]
	s_add_u32 s12, s12, s8
	s_addc_u32 s13, s13, s9
	v_lshlrev_b32_e32 v6, 4, v1
	v_bfe_u32 v16, v2, 0, 1
	v_lshl_or_b32 v6, v16, 12, v6
	v_bfe_u32 v16, v2, 1, 1
	v_lshl_or_b32 v6, v16, 13, v6
	v_bfe_u32 v16, v2, 2, 1
	v_lshl_or_b32 v6, v16, 14, v6
	global_load_dwordx4 v[128:131], v6, s[12:13] offset:0 nt
	global_load_dwordx4 v[132:135], v6, s[12:13] offset:1024 nt
	global_load_dwordx4 v[136:139], v6, s[12:13] offset:2048 nt
	global_load_dwordx4 v[140:143], v6, s[12:13] offset:3072 nt
	v_add_u32_e32 v6, 0x8000, v6
	global_load_dwordx4 v[144:147], v6, s[12:13] offset:0 nt
	global_load_dwordx4 v[148:151], v6, s[12:13] offset:1024 nt
	global_load_dwordx4 v[152:155], v6, s[12:13] offset:2048 nt
	global_load_dwordx4 v[156:159], v6, s[12:13] offset:3072 nt
	v_add_u32_e32 v6, 0x8000, v6
	global_load_dwordx4 v[160:163], v6, s[12:13] offset:0 nt
	global_load_dwordx4 v[164:167], v6, s[12:13] offset:1024 nt
	global_load_dwordx4 v[168:171], v6, s[12:13] offset:2048 nt
	global_load_dwordx4 v[172:175], v6, s[12:13] offset:3072 nt
	v_add_u32_e32 v6, 0x8000, v6
	global_load_dwordx4 v[176:179], v6, s[12:13] offset:0 nt
	global_load_dwordx4 v[180:183], v6, s[12:13] offset:1024 nt
	global_load_dwordx4 v[184:187], v6, s[12:13] offset:2048 nt
	global_load_dwordx4 v[188:191], v6, s[12:13] offset:3072 nt
	v_add_u32_e32 v6, 0x8000, v6
	global_load_dwordx4 v[192:195], v6, s[12:13] offset:0 nt
	global_load_dwordx4 v[196:199], v6, s[12:13] offset:1024 nt
	global_load_dwordx4 v[200:203], v6, s[12:13] offset:2048 nt
	global_load_dwordx4 v[204:207], v6, s[12:13] offset:3072 nt
	v_add_u32_e32 v6, 0x8000, v6
	global_load_dwordx4 v[208:211], v6, s[12:13] offset:0 nt
	global_load_dwordx4 v[212:215], v6, s[12:13] offset:1024 nt
	global_load_dwordx4 v[216:219], v6, s[12:13] offset:2048 nt
	global_load_dwordx4 v[220:223], v6, s[12:13] offset:3072 nt
	v_add_u32_e32 v6, 0x8000, v6
	global_load_dwordx4 v[224:227], v6, s[12:13] offset:0 nt
	global_load_dwordx4 v[228:231], v6, s[12:13] offset:1024 nt
	global_load_dwordx4 v[232:235], v6, s[12:13] offset:2048 nt
	global_load_dwordx4 v[236:239], v6, s[12:13] offset:3072 nt
	v_add_u32_e32 v6, 0x8000, v6
	global_load_dwordx4 v[240:243], v6, s[12:13] offset:0 nt
	global_load_dwordx4 v[244:247], v6, s[12:13] offset:1024 nt
	global_load_dwordx4 v[248:251], v6, s[12:13] offset:2048 nt
	global_load_dwordx4 v[252:255], v6, s[12:13] offset:3072 nt
	v_and_b32_e32 v16, 1, v0
	v_cmp_eq_u32_e64 s[30:31], 0, v16
	v_and_b32_e32 v17, 2, v0
	v_cmp_eq_u32_e64 s[32:33], 0, v17
	v_lshrrev_b32_e32 v17, 2, v1
	v_lshlrev_b32_e32 v14, 1, v17
	v_bfe_u32 v16, v2, 0, 1
	s_movk_i32 s10, 0x80
	v_mad_u32_u24 v14, v16, s10, v14
	v_bfe_u32 v16, v2, 1, 1
	s_movk_i32 s10, 0x110
	v_mad_u32_u24 v14, v16, s10, v14
	v_bfe_u32 v16, v2, 2, 1
	s_movk_i32 s10, 0x220
	v_mad_u32_u24 v14, v16, s10, v14
	v_bfe_u32 v16, v0, 0, 1
	s_movk_i32 s10, 0x20
	v_mad_u32_u24 v14, v16, s10, v14
	v_bfe_u32 v16, v0, 1, 1
	s_movk_i32 s10, 0x40
	v_mad_u32_u24 v14, v16, s10, v14
	s_movk_i32 s10, 0x110
	v_lshlrev_b32_e32 v17, 4, v7
	v_mad_u32_u24 v15, v3, s10, v17
	s_lshl_b32 s11, s6, 5
	v_lshl_add_u32 v18, v7, 2, s11
	v_cvt_f32_u32_e32 v18, v18
	v_lshlrev_b32_e32 v19, 3, v7
	v_cvt_f32_u32_e32 v19, v19
	s_waitcnt vmcnt(32)
	v_add_f32_e32 v26, v20, v21
	v_rcp_f32_e32 v27, v20
	v_rcp_f32_e32 v28, v26
	v_sub_f32_e32 v12, v19, v22
	v_sub_f32_e32 v13, v18, v23
	v_fma_f32 v29, -v20, v27, 1.0
	v_fma_f32 v30, -v26, v28, 1.0
	v_fma_f32 v27, v29, v27, v27
	v_fma_f32 v28, v30, v28, v28
	v_mul_f32_e32 v8, 0xbf38aa3b, v27
	v_mul_f32_e32 v9, 0xbf38aa3b, v28
	v_mul_f32_e32 v29, v24, v27
	v_mul_f32_e32 v30, v25, v28
	v_mul_f32_e32 v10, 0x3e22f983, v29
	v_mul_f32_e32 v11, 0x3e22f983, v30
	v_mul_f32_e32 v16, v12, v12
	v_add_f32_e32 v17, 0x3f800000, v12
	v_add_f32_e32 v18, 0x40000000, v12
	v_add_f32_e32 v19, 0x40400000, v12
	v_mul_f32_e32 v17, v17, v17
	v_mul_f32_e32 v18, v18, v18
	v_mul_f32_e32 v19, v19, v19
	v_mul_f32_e32 v20, v8, v16
	v_mul_f32_e32 v24, v9, v16
	v_mul_f32_e32 v21, v8, v17
	v_mul_f32_e32 v25, v9, v17
	v_mul_f32_e32 v22, v8, v18
	v_mul_f32_e32 v26, v9, v18
	v_mul_f32_e32 v23, v8, v19
	v_mul_f32_e32 v27, v9, v19
	v_exp_f32_e32 v20, v20
	v_exp_f32_e32 v21, v21
	v_exp_f32_e32 v22, v22
	v_exp_f32_e32 v23, v23
	v_exp_f32_e32 v24, v24
	v_exp_f32_e32 v25, v25
	v_exp_f32_e32 v26, v26
	v_exp_f32_e32 v27, v27
	v_cvt_pk_f16_f32 v32, v20, v21
	v_cvt_pk_f16_f32 v33, v22, v23
	v_cvt_pk_f16_f32 v64, v24, v25
	v_cvt_pk_f16_f32 v65, v26, v27
	v_add_f32_e32 v16, 0x40800000, v12
	v_add_f32_e32 v17, 0x40a00000, v12
	v_add_f32_e32 v18, 0x40c00000, v12
	v_add_f32_e32 v19, 0x40e00000, v12
	v_mul_f32_e32 v16, v16, v16
	v_mul_f32_e32 v17, v17, v17
	v_mul_f32_e32 v18, v18, v18
	v_mul_f32_e32 v19, v19, v19
	v_mul_f32_e32 v20, v8, v16
	v_mul_f32_e32 v24, v9, v16
	v_mul_f32_e32 v21, v8, v17
	v_mul_f32_e32 v25, v9, v17
	v_mul_f32_e32 v22, v8, v18
	v_mul_f32_e32 v26, v9, v18
	v_mul_f32_e32 v23, v8, v19
	v_mul_f32_e32 v27, v9, v19
	v_exp_f32_e32 v20, v20
	v_exp_f32_e32 v21, v21
	v_exp_f32_e32 v22, v22
	v_exp_f32_e32 v23, v23
	v_exp_f32_e32 v24, v24
	v_exp_f32_e32 v25, v25
	v_exp_f32_e32 v26, v26
	v_exp_f32_e32 v27, v27
	v_cvt_pk_f16_f32 v34, v20, v21
	v_cvt_pk_f16_f32 v35, v22, v23
	v_cvt_pk_f16_f32 v66, v24, v25
	v_cvt_pk_f16_f32 v67, v26, v27
	v_add_f32_e32 v16, 0x41800000, v12
	v_add_f32_e32 v17, 0x41880000, v12
	v_add_f32_e32 v18, 0x41900000, v12
	v_add_f32_e32 v19, 0x41980000, v12
	v_mul_f32_e32 v16, v16, v16
	v_mul_f32_e32 v17, v17, v17
	v_mul_f32_e32 v18, v18, v18
	v_mul_f32_e32 v19, v19, v19
	v_mul_f32_e32 v20, v8, v16
	v_mul_f32_e32 v24, v9, v16
	v_mul_f32_e32 v21, v8, v17
	v_mul_f32_e32 v25, v9, v17
	v_mul_f32_e32 v22, v8, v18
	v_mul_f32_e32 v26, v9, v18
	v_mul_f32_e32 v23, v8, v19
	v_mul_f32_e32 v27, v9, v19
	v_exp_f32_e32 v20, v20
	v_exp_f32_e32 v21, v21
	v_exp_f32_e32 v22, v22
	v_exp_f32_e32 v23, v23
	v_exp_f32_e32 v24, v24
	v_exp_f32_e32 v25, v25
	v_exp_f32_e32 v26, v26
	v_exp_f32_e32 v27, v27
	v_cvt_pk_f16_f32 v36, v20, v21
	v_cvt_pk_f16_f32 v37, v22, v23
	v_cvt_pk_f16_f32 v68, v24, v25
	v_cvt_pk_f16_f32 v69, v26, v27
	v_add_f32_e32 v16, 0x41a00000, v12
	v_add_f32_e32 v17, 0x41a80000, v12
	v_add_f32_e32 v18, 0x41b00000, v12
	v_add_f32_e32 v19, 0x41b80000, v12
	v_mul_f32_e32 v16, v16, v16
	v_mul_f32_e32 v17, v17, v17
	v_mul_f32_e32 v18, v18, v18
	v_mul_f32_e32 v19, v19, v19
	v_mul_f32_e32 v20, v8, v16
	v_mul_f32_e32 v24, v9, v16
	v_mul_f32_e32 v21, v8, v17
	v_mul_f32_e32 v25, v9, v17
	v_mul_f32_e32 v22, v8, v18
	v_mul_f32_e32 v26, v9, v18
	v_mul_f32_e32 v23, v8, v19
	v_mul_f32_e32 v27, v9, v19
	v_exp_f32_e32 v20, v20
	v_exp_f32_e32 v21, v21
	v_exp_f32_e32 v22, v22
	v_exp_f32_e32 v23, v23
	v_exp_f32_e32 v24, v24
	v_exp_f32_e32 v25, v25
	v_exp_f32_e32 v26, v26
	v_exp_f32_e32 v27, v27
	v_cvt_pk_f16_f32 v38, v20, v21
	v_cvt_pk_f16_f32 v39, v22, v23
	v_cvt_pk_f16_f32 v70, v24, v25
	v_cvt_pk_f16_f32 v71, v26, v27
	v_add_f32_e32 v16, 0x42000000, v12
	v_add_f32_e32 v17, 0x42040000, v12
	v_add_f32_e32 v18, 0x42080000, v12
	v_add_f32_e32 v19, 0x420c0000, v12
	v_mul_f32_e32 v16, v16, v16
	v_mul_f32_e32 v17, v17, v17
	v_mul_f32_e32 v18, v18, v18
	v_mul_f32_e32 v19, v19, v19
	v_mul_f32_e32 v20, v8, v16
	v_mul_f32_e32 v24, v9, v16
	v_mul_f32_e32 v21, v8, v17
	v_mul_f32_e32 v25, v9, v17
	v_mul_f32_e32 v22, v8, v18
	v_mul_f32_e32 v26, v9, v18
	v_mul_f32_e32 v23, v8, v19
	v_mul_f32_e32 v27, v9, v19
	v_exp_f32_e32 v20, v20
	v_exp_f32_e32 v21, v21
	v_exp_f32_e32 v22, v22
	v_exp_f32_e32 v23, v23
	v_exp_f32_e32 v24, v24
	v_exp_f32_e32 v25, v25
	v_exp_f32_e32 v26, v26
	v_exp_f32_e32 v27, v27
	v_cvt_pk_f16_f32 v40, v20, v21
	v_cvt_pk_f16_f32 v41, v22, v23
	v_cvt_pk_f16_f32 v72, v24, v25
	v_cvt_pk_f16_f32 v73, v26, v27
	v_add_f32_e32 v16, 0x42100000, v12
	v_add_f32_e32 v17, 0x42140000, v12
	v_add_f32_e32 v18, 0x42180000, v12
	v_add_f32_e32 v19, 0x421c0000, v12
	v_mul_f32_e32 v16, v16, v16
	v_mul_f32_e32 v17, v17, v17
	v_mul_f32_e32 v18, v18, v18
	v_mul_f32_e32 v19, v19, v19
	v_mul_f32_e32 v20, v8, v16
	v_mul_f32_e32 v24, v9, v16
	v_mul_f32_e32 v21, v8, v17
	v_mul_f32_e32 v25, v9, v17
	v_mul_f32_e32 v22, v8, v18
	v_mul_f32_e32 v26, v9, v18
	v_mul_f32_e32 v23, v8, v19
	v_mul_f32_e32 v27, v9, v19
	v_exp_f32_e32 v20, v20
	v_exp_f32_e32 v21, v21
	v_exp_f32_e32 v22, v22
	v_exp_f32_e32 v23, v23
	v_exp_f32_e32 v24, v24
	v_exp_f32_e32 v25, v25
	v_exp_f32_e32 v26, v26
	v_exp_f32_e32 v27, v27
	v_cvt_pk_f16_f32 v42, v20, v21
	v_cvt_pk_f16_f32 v43, v22, v23
	v_cvt_pk_f16_f32 v74, v24, v25
	v_cvt_pk_f16_f32 v75, v26, v27
	v_add_f32_e32 v16, 0x42400000, v12
	v_add_f32_e32 v17, 0x42440000, v12
	v_add_f32_e32 v18, 0x42480000, v12
	v_add_f32_e32 v19, 0x424c0000, v12
	v_mul_f32_e32 v16, v16, v16
	v_mul_f32_e32 v17, v17, v17
	v_mul_f32_e32 v18, v18, v18
	v_mul_f32_e32 v19, v19, v19
	v_mul_f32_e32 v20, v8, v16
	v_mul_f32_e32 v24, v9, v16
	v_mul_f32_e32 v21, v8, v17
	v_mul_f32_e32 v25, v9, v17
	v_mul_f32_e32 v22, v8, v18
	v_mul_f32_e32 v26, v9, v18
	v_mul_f32_e32 v23, v8, v19
	v_mul_f32_e32 v27, v9, v19
	v_exp_f32_e32 v20, v20
	v_exp_f32_e32 v21, v21
	v_exp_f32_e32 v22, v22
	v_exp_f32_e32 v23, v23
	v_exp_f32_e32 v24, v24
	v_exp_f32_e32 v25, v25
	v_exp_f32_e32 v26, v26
	v_exp_f32_e32 v27, v27
	v_cvt_pk_f16_f32 v44, v20, v21
	v_cvt_pk_f16_f32 v45, v22, v23
	v_cvt_pk_f16_f32 v76, v24, v25
	v_cvt_pk_f16_f32 v77, v26, v27
	v_add_f32_e32 v16, 0x42500000, v12
	v_add_f32_e32 v17, 0x42540000, v12
	v_add_f32_e32 v18, 0x42580000, v12
	v_add_f32_e32 v19, 0x425c0000, v12
	v_mul_f32_e32 v16, v16, v16
	v_mul_f32_e32 v17, v17, v17
	v_mul_f32_e32 v18, v18, v18
	v_mul_f32_e32 v19, v19, v19
	v_mul_f32_e32 v20, v8, v16
	v_mul_f32_e32 v24, v9, v16
	v_mul_f32_e32 v21, v8, v17
	v_mul_f32_e32 v25, v9, v17
	v_mul_f32_e32 v22, v8, v18
	v_mul_f32_e32 v26, v9, v18
	v_mul_f32_e32 v23, v8, v19
	v_mul_f32_e32 v27, v9, v19
	v_exp_f32_e32 v20, v20
	v_exp_f32_e32 v21, v21
	v_exp_f32_e32 v22, v22
	v_exp_f32_e32 v23, v23
	v_exp_f32_e32 v24, v24
	v_exp_f32_e32 v25, v25
	v_exp_f32_e32 v26, v26
	v_exp_f32_e32 v27, v27
	v_cvt_pk_f16_f32 v46, v20, v21
	v_cvt_pk_f16_f32 v47, v22, v23
	v_cvt_pk_f16_f32 v78, v24, v25
	v_cvt_pk_f16_f32 v79, v26, v27
	v_add_f32_e32 v16, 0x42800000, v12
	v_add_f32_e32 v17, 0x42820000, v12
	v_add_f32_e32 v18, 0x42840000, v12
	v_add_f32_e32 v19, 0x42860000, v12
	v_mul_f32_e32 v16, v16, v16
	v_mul_f32_e32 v17, v17, v17
	v_mul_f32_e32 v18, v18, v18
	v_mul_f32_e32 v19, v19, v19
	v_mul_f32_e32 v20, v8, v16
	v_mul_f32_e32 v24, v9, v16
	v_mul_f32_e32 v21, v8, v17
	v_mul_f32_e32 v25, v9, v17
	v_mul_f32_e32 v22, v8, v18
	v_mul_f32_e32 v26, v9, v18
	v_mul_f32_e32 v23, v8, v19
	v_mul_f32_e32 v27, v9, v19
	v_exp_f32_e32 v20, v20
	v_exp_f32_e32 v21, v21
	v_exp_f32_e32 v22, v22
	v_exp_f32_e32 v23, v23
	v_exp_f32_e32 v24, v24
	v_exp_f32_e32 v25, v25
	v_exp_f32_e32 v26, v26
	v_exp_f32_e32 v27, v27
	v_cvt_pk_f16_f32 v48, v20, v21
	v_cvt_pk_f16_f32 v49, v22, v23
	v_cvt_pk_f16_f32 v80, v24, v25
	v_cvt_pk_f16_f32 v81, v26, v27
	v_add_f32_e32 v16, 0x42880000, v12
	v_add_f32_e32 v17, 0x428a0000, v12
	v_add_f32_e32 v18, 0x428c0000, v12
	v_add_f32_e32 v19, 0x428e0000, v12
	v_mul_f32_e32 v16, v16, v16
	v_mul_f32_e32 v17, v17, v17
	v_mul_f32_e32 v18, v18, v18
	v_mul_f32_e32 v19, v19, v19
	v_mul_f32_e32 v20, v8, v16
	v_mul_f32_e32 v24, v9, v16
	v_mul_f32_e32 v21, v8, v17
	v_mul_f32_e32 v25, v9, v17
	v_mul_f32_e32 v22, v8, v18
	v_mul_f32_e32 v26, v9, v18
	v_mul_f32_e32 v23, v8, v19
	v_mul_f32_e32 v27, v9, v19
	v_exp_f32_e32 v20, v20
	v_exp_f32_e32 v21, v21
	v_exp_f32_e32 v22, v22
	v_exp_f32_e32 v23, v23
	v_exp_f32_e32 v24, v24
	v_exp_f32_e32 v25, v25
	v_exp_f32_e32 v26, v26
	v_exp_f32_e32 v27, v27
	v_cvt_pk_f16_f32 v50, v20, v21
	v_cvt_pk_f16_f32 v51, v22, v23
	v_cvt_pk_f16_f32 v82, v24, v25
	v_cvt_pk_f16_f32 v83, v26, v27
	v_add_f32_e32 v16, 0x42a00000, v12
	v_add_f32_e32 v17, 0x42a20000, v12
	v_add_f32_e32 v18, 0x42a40000, v12
	v_add_f32_e32 v19, 0x42a60000, v12
	v_mul_f32_e32 v16, v16, v16
	v_mul_f32_e32 v17, v17, v17
	v_mul_f32_e32 v18, v18, v18
	v_mul_f32_e32 v19, v19, v19
	v_mul_f32_e32 v20, v8, v16
	v_mul_f32_e32 v24, v9, v16
	v_mul_f32_e32 v21, v8, v17
	v_mul_f32_e32 v25, v9, v17
	v_mul_f32_e32 v22, v8, v18
	v_mul_f32_e32 v26, v9, v18
	v_mul_f32_e32 v23, v8, v19
	v_mul_f32_e32 v27, v9, v19
	v_exp_f32_e32 v20, v20
	v_exp_f32_e32 v21, v21
	v_exp_f32_e32 v22, v22
	v_exp_f32_e32 v23, v23
	v_exp_f32_e32 v24, v24
	v_exp_f32_e32 v25, v25
	v_exp_f32_e32 v26, v26
	v_exp_f32_e32 v27, v27
	v_cvt_pk_f16_f32 v52, v20, v21
	v_cvt_pk_f16_f32 v53, v22, v23
	v_cvt_pk_f16_f32 v84, v24, v25
	v_cvt_pk_f16_f32 v85, v26, v27
	v_add_f32_e32 v16, 0x42a80000, v12
	v_add_f32_e32 v17, 0x42aa0000, v12
	v_add_f32_e32 v18, 0x42ac0000, v12
	v_add_f32_e32 v19, 0x42ae0000, v12
	v_mul_f32_e32 v16, v16, v16
	v_mul_f32_e32 v17, v17, v17
	v_mul_f32_e32 v18, v18, v18
	v_mul_f32_e32 v19, v19, v19
	v_mul_f32_e32 v20, v8, v16
	v_mul_f32_e32 v24, v9, v16
	v_mul_f32_e32 v21, v8, v17
	v_mul_f32_e32 v25, v9, v17
	v_mul_f32_e32 v22, v8, v18
	v_mul_f32_e32 v26, v9, v18
	v_mul_f32_e32 v23, v8, v19
	v_mul_f32_e32 v27, v9, v19
	v_exp_f32_e32 v20, v20
	v_exp_f32_e32 v21, v21
	v_exp_f32_e32 v22, v22
	v_exp_f32_e32 v23, v23
	v_exp_f32_e32 v24, v24
	v_exp_f32_e32 v25, v25
	v_exp_f32_e32 v26, v26
	v_exp_f32_e32 v27, v27
	v_cvt_pk_f16_f32 v54, v20, v21
	v_cvt_pk_f16_f32 v55, v22, v23
	v_cvt_pk_f16_f32 v86, v24, v25
	v_cvt_pk_f16_f32 v87, v26, v27
	v_add_f32_e32 v16, 0x42c00000, v12
	v_add_f32_e32 v17, 0x42c20000, v12
	v_add_f32_e32 v18, 0x42c40000, v12
	v_add_f32_e32 v19, 0x42c60000, v12
	v_mul_f32_e32 v16, v16, v16
	v_mul_f32_e32 v17, v17, v17
	v_mul_f32_e32 v18, v18, v18
	v_mul_f32_e32 v19, v19, v19
	v_mul_f32_e32 v20, v8, v16
	v_mul_f32_e32 v24, v9, v16
	v_mul_f32_e32 v21, v8, v17
	v_mul_f32_e32 v25, v9, v17
	v_mul_f32_e32 v22, v8, v18
	v_mul_f32_e32 v26, v9, v18
	v_mul_f32_e32 v23, v8, v19
	v_mul_f32_e32 v27, v9, v19
	v_exp_f32_e32 v20, v20
	v_exp_f32_e32 v21, v21
	v_exp_f32_e32 v22, v22
	v_exp_f32_e32 v23, v23
	v_exp_f32_e32 v24, v24
	v_exp_f32_e32 v25, v25
	v_exp_f32_e32 v26, v26
	v_exp_f32_e32 v27, v27
	v_cvt_pk_f16_f32 v56, v20, v21
	v_cvt_pk_f16_f32 v57, v22, v23
	v_cvt_pk_f16_f32 v88, v24, v25
	v_cvt_pk_f16_f32 v89, v26, v27
	v_add_f32_e32 v16, 0x42c80000, v12
	v_add_f32_e32 v17, 0x42ca0000, v12
	v_add_f32_e32 v18, 0x42cc0000, v12
	v_add_f32_e32 v19, 0x42ce0000, v12
	v_mul_f32_e32 v16, v16, v16
	v_mul_f32_e32 v17, v17, v17
	v_mul_f32_e32 v18, v18, v18
	v_mul_f32_e32 v19, v19, v19
	v_mul_f32_e32 v20, v8, v16
	v_mul_f32_e32 v24, v9, v16
	v_mul_f32_e32 v21, v8, v17
	v_mul_f32_e32 v25, v9, v17
	v_mul_f32_e32 v22, v8, v18
	v_mul_f32_e32 v26, v9, v18
	v_mul_f32_e32 v23, v8, v19
	v_mul_f32_e32 v27, v9, v19
	v_exp_f32_e32 v20, v20
	v_exp_f32_e32 v21, v21
	v_exp_f32_e32 v22, v22
	v_exp_f32_e32 v23, v23
	v_exp_f32_e32 v24, v24
	v_exp_f32_e32 v25, v25
	v_exp_f32_e32 v26, v26
	v_exp_f32_e32 v27, v27
	v_cvt_pk_f16_f32 v58, v20, v21
	v_cvt_pk_f16_f32 v59, v22, v23
	v_cvt_pk_f16_f32 v90, v24, v25
	v_cvt_pk_f16_f32 v91, v26, v27
	v_add_f32_e32 v16, 0x42e00000, v12
	v_add_f32_e32 v17, 0x42e20000, v12
	v_add_f32_e32 v18, 0x42e40000, v12
	v_add_f32_e32 v19, 0x42e60000, v12
	v_mul_f32_e32 v16, v16, v16
	v_mul_f32_e32 v17, v17, v17
	v_mul_f32_e32 v18, v18, v18
	v_mul_f32_e32 v19, v19, v19
	v_mul_f32_e32 v20, v8, v16
	v_mul_f32_e32 v24, v9, v16
	v_mul_f32_e32 v21, v8, v17
	v_mul_f32_e32 v25, v9, v17
	v_mul_f32_e32 v22, v8, v18
	v_mul_f32_e32 v26, v9, v18
	v_mul_f32_e32 v23, v8, v19
	v_mul_f32_e32 v27, v9, v19
	v_exp_f32_e32 v20, v20
	v_exp_f32_e32 v21, v21
	v_exp_f32_e32 v22, v22
	v_exp_f32_e32 v23, v23
	v_exp_f32_e32 v24, v24
	v_exp_f32_e32 v25, v25
	v_exp_f32_e32 v26, v26
	v_exp_f32_e32 v27, v27
	v_cvt_pk_f16_f32 v60, v20, v21
	v_cvt_pk_f16_f32 v61, v22, v23
	v_cvt_pk_f16_f32 v92, v24, v25
	v_cvt_pk_f16_f32 v93, v26, v27
	v_add_f32_e32 v16, 0x42e80000, v12
	v_add_f32_e32 v17, 0x42ea0000, v12
	v_add_f32_e32 v18, 0x42ec0000, v12
	v_add_f32_e32 v19, 0x42ee0000, v12
	v_mul_f32_e32 v16, v16, v16
	v_mul_f32_e32 v17, v17, v17
	v_mul_f32_e32 v18, v18, v18
	v_mul_f32_e32 v19, v19, v19
	v_mul_f32_e32 v20, v8, v16
	v_mul_f32_e32 v24, v9, v16
	v_mul_f32_e32 v21, v8, v17
	v_mul_f32_e32 v25, v9, v17
	v_mul_f32_e32 v22, v8, v18
	v_mul_f32_e32 v26, v9, v18
	v_mul_f32_e32 v23, v8, v19
	v_mul_f32_e32 v27, v9, v19
	v_exp_f32_e32 v20, v20
	v_exp_f32_e32 v21, v21
	v_exp_f32_e32 v22, v22
	v_exp_f32_e32 v23, v23
	v_exp_f32_e32 v24, v24
	v_exp_f32_e32 v25, v25
	v_exp_f32_e32 v26, v26
	v_exp_f32_e32 v27, v27
	v_cvt_pk_f16_f32 v62, v20, v21
	v_cvt_pk_f16_f32 v63, v22, v23
	v_cvt_pk_f16_f32 v94, v24, v25
	v_cvt_pk_f16_f32 v95, v26, v27
	v_mul_f32_e32 v16, v13, v13
	v_add_f32_e32 v17, 0x3f800000, v13
	v_add_f32_e32 v18, 0x40000000, v13
	v_add_f32_e32 v19, 0x40400000, v13
	v_mul_f32_e32 v17, v17, v17
	v_mul_f32_e32 v18, v18, v18
	v_mul_f32_e32 v19, v19, v19
	v_mul_f32_e32 v20, v8, v16
	v_mul_f32_e32 v24, v9, v16
	v_mul_f32_e32 v21, v8, v17
	v_mul_f32_e32 v25, v9, v17
	v_mul_f32_e32 v22, v8, v18
	v_mul_f32_e32 v26, v9, v18
	v_mul_f32_e32 v23, v8, v19
	v_mul_f32_e32 v27, v9, v19
	v_exp_f32_e32 v20, v20
	v_exp_f32_e32 v21, v21
	v_exp_f32_e32 v22, v22
	v_exp_f32_e32 v23, v23
	v_exp_f32_e32 v24, v24
	v_exp_f32_e32 v25, v25
	v_exp_f32_e32 v26, v26
	v_exp_f32_e32 v27, v27
	v_mul_f32_e32 v96, v10, v20
	v_mul_f32_e32 v97, v10, v21
	v_mul_f32_e32 v98, v10, v22
	v_mul_f32_e32 v99, v10, v23
	v_mul_f32_e32 v112, v11, v24
	v_mul_f32_e32 v113, v11, v25
	v_mul_f32_e32 v114, v11, v26
	v_mul_f32_e32 v115, v11, v27
	v_add_f32_e32 v16, 0x41000000, v13
	v_add_f32_e32 v17, 0x41100000, v13
	v_add_f32_e32 v18, 0x41200000, v13
	v_add_f32_e32 v19, 0x41300000, v13
	v_mul_f32_e32 v16, v16, v16
	v_mul_f32_e32 v17, v17, v17
	v_mul_f32_e32 v18, v18, v18
	v_mul_f32_e32 v19, v19, v19
	v_mul_f32_e32 v20, v8, v16
	v_mul_f32_e32 v24, v9, v16
	v_mul_f32_e32 v21, v8, v17
	v_mul_f32_e32 v25, v9, v17
	v_mul_f32_e32 v22, v8, v18
	v_mul_f32_e32 v26, v9, v18
	v_mul_f32_e32 v23, v8, v19
	v_mul_f32_e32 v27, v9, v19
	v_exp_f32_e32 v20, v20
	v_exp_f32_e32 v21, v21
	v_exp_f32_e32 v22, v22
	v_exp_f32_e32 v23, v23
	v_exp_f32_e32 v24, v24
	v_exp_f32_e32 v25, v25
	v_exp_f32_e32 v26, v26
	v_exp_f32_e32 v27, v27
	v_mul_f32_e32 v100, v10, v20
	v_mul_f32_e32 v101, v10, v21
	v_mul_f32_e32 v102, v10, v22
	v_mul_f32_e32 v103, v10, v23
	v_mul_f32_e32 v116, v11, v24
	v_mul_f32_e32 v117, v11, v25
	v_mul_f32_e32 v118, v11, v26
	v_mul_f32_e32 v119, v11, v27
	v_add_f32_e32 v16, 0x41800000, v13
	v_add_f32_e32 v17, 0x41880000, v13
	v_add_f32_e32 v18, 0x41900000, v13
	v_add_f32_e32 v19, 0x41980000, v13
	v_mul_f32_e32 v16, v16, v16
	v_mul_f32_e32 v17, v17, v17
	v_mul_f32_e32 v18, v18, v18
	v_mul_f32_e32 v19, v19, v19
	v_mul_f32_e32 v20, v8, v16
	v_mul_f32_e32 v24, v9, v16
	v_mul_f32_e32 v21, v8, v17
	v_mul_f32_e32 v25, v9, v17
	v_mul_f32_e32 v22, v8, v18
	v_mul_f32_e32 v26, v9, v18
	v_mul_f32_e32 v23, v8, v19
	v_mul_f32_e32 v27, v9, v19
	v_exp_f32_e32 v20, v20
	v_exp_f32_e32 v21, v21
	v_exp_f32_e32 v22, v22
	v_exp_f32_e32 v23, v23
	v_exp_f32_e32 v24, v24
	v_exp_f32_e32 v25, v25
	v_exp_f32_e32 v26, v26
	v_exp_f32_e32 v27, v27
	v_mul_f32_e32 v104, v10, v20
	v_mul_f32_e32 v105, v10, v21
	v_mul_f32_e32 v106, v10, v22
	v_mul_f32_e32 v107, v10, v23
	v_mul_f32_e32 v120, v11, v24
	v_mul_f32_e32 v121, v11, v25
	v_mul_f32_e32 v122, v11, v26
	v_mul_f32_e32 v123, v11, v27
	v_add_f32_e32 v16, 0x41c00000, v13
	v_add_f32_e32 v17, 0x41c80000, v13
	v_add_f32_e32 v18, 0x41d00000, v13
	v_add_f32_e32 v19, 0x41d80000, v13
	v_mul_f32_e32 v16, v16, v16
	v_mul_f32_e32 v17, v17, v17
	v_mul_f32_e32 v18, v18, v18
	v_mul_f32_e32 v19, v19, v19
	v_mul_f32_e32 v20, v8, v16
	v_mul_f32_e32 v24, v9, v16
	v_mul_f32_e32 v21, v8, v17
	v_mul_f32_e32 v25, v9, v17
	v_mul_f32_e32 v22, v8, v18
	v_mul_f32_e32 v26, v9, v18
	v_mul_f32_e32 v23, v8, v19
	v_mul_f32_e32 v27, v9, v19
	v_exp_f32_e32 v20, v20
	v_exp_f32_e32 v21, v21
	v_exp_f32_e32 v22, v22
	v_exp_f32_e32 v23, v23
	v_exp_f32_e32 v24, v24
	v_exp_f32_e32 v25, v25
	v_exp_f32_e32 v26, v26
	v_exp_f32_e32 v27, v27
	v_mul_f32_e32 v108, v10, v20
	v_mul_f32_e32 v109, v10, v21
	v_mul_f32_e32 v110, v10, v22
	v_mul_f32_e32 v111, v10, v23
	v_mul_f32_e32 v124, v11, v24
	v_mul_f32_e32 v125, v11, v25
	v_mul_f32_e32 v126, v11, v26
	v_mul_f32_e32 v127, v11, v27
	s_waitcnt vmcnt(28)
	v_add_f32_e32 v128, v128, v129
	v_add_f32_e32 v130, v130, v131
	v_add_f32_e32 v132, v132, v133
	v_add_f32_e32 v134, v134, v135
	v_add_f32_e32 v136, v136, v137
	v_add_f32_e32 v138, v138, v139
	v_add_f32_e32 v140, v140, v141
	v_add_f32_e32 v142, v142, v143
	v_add_f32_e32 v128, v128, v130
	v_add_f32_e32 v132, v132, v134
	v_add_f32_e32 v136, v136, v138
	v_add_f32_e32 v140, v140, v142
	v_cndmask_b32_e64 v130, v128, v132, s[30:31]
	v_cndmask_b32_e64 v134, v136, v140, s[30:31]
	v_cndmask_b32_e64 v129, v132, v128, s[30:31]
	v_cndmask_b32_e64 v133, v140, v136, s[30:31]
	v_add_f32_dpp v129, v130, v129 quad_perm:[1,0,3,2] row_mask:0xf bank_mask:0xf bound_ctrl:1
	v_add_f32_dpp v133, v134, v133 quad_perm:[1,0,3,2] row_mask:0xf bank_mask:0xf bound_ctrl:1
	v_cndmask_b32_e64 v135, v129, v133, s[32:33]
	v_cndmask_b32_e64 v131, v133, v129, s[32:33]
	s_nop 1
	v_add_f32_dpp v131, v135, v131 quad_perm:[2,3,0,1] row_mask:0xf bank_mask:0xf bound_ctrl:1
	v_cvt_f16_f32_e32 v131, v131
	ds_write_b16 v14, v131 offset:0
	s_waitcnt vmcnt(24)
	v_add_f32_e32 v144, v144, v145
	v_add_f32_e32 v146, v146, v147
	v_add_f32_e32 v148, v148, v149
	v_add_f32_e32 v150, v150, v151
	v_add_f32_e32 v152, v152, v153
	v_add_f32_e32 v154, v154, v155
	v_add_f32_e32 v156, v156, v157
	v_add_f32_e32 v158, v158, v159
	v_add_f32_e32 v144, v144, v146
	v_add_f32_e32 v148, v148, v150
	v_add_f32_e32 v152, v152, v154
	v_add_f32_e32 v156, v156, v158
	v_cndmask_b32_e64 v146, v144, v148, s[30:31]
	v_cndmask_b32_e64 v150, v152, v156, s[30:31]
	v_cndmask_b32_e64 v145, v148, v144, s[30:31]
	v_cndmask_b32_e64 v149, v156, v152, s[30:31]
	v_add_f32_dpp v145, v146, v145 quad_perm:[1,0,3,2] row_mask:0xf bank_mask:0xf bound_ctrl:1
	v_add_f32_dpp v149, v150, v149 quad_perm:[1,0,3,2] row_mask:0xf bank_mask:0xf bound_ctrl:1
	v_cndmask_b32_e64 v151, v145, v149, s[32:33]
	v_cndmask_b32_e64 v147, v149, v145, s[32:33]
	s_nop 1
	v_add_f32_dpp v147, v151, v147 quad_perm:[2,3,0,1] row_mask:0xf bank_mask:0xf bound_ctrl:1
	v_cvt_f16_f32_e32 v147, v147
	ds_write_b16 v14, v147 offset:1088
	s_waitcnt vmcnt(20)
	v_add_f32_e32 v160, v160, v161
	v_add_f32_e32 v162, v162, v163
	v_add_f32_e32 v164, v164, v165
	v_add_f32_e32 v166, v166, v167
	v_add_f32_e32 v168, v168, v169
	v_add_f32_e32 v170, v170, v171
	v_add_f32_e32 v172, v172, v173
	v_add_f32_e32 v174, v174, v175
	v_add_f32_e32 v160, v160, v162
	v_add_f32_e32 v164, v164, v166
	v_add_f32_e32 v168, v168, v170
	v_add_f32_e32 v172, v172, v174
	v_cndmask_b32_e64 v162, v160, v164, s[30:31]
	v_cndmask_b32_e64 v166, v168, v172, s[30:31]
	v_cndmask_b32_e64 v161, v164, v160, s[30:31]
	v_cndmask_b32_e64 v165, v172, v168, s[30:31]
	v_add_f32_dpp v161, v162, v161 quad_perm:[1,0,3,2] row_mask:0xf bank_mask:0xf bound_ctrl:1
	v_add_f32_dpp v165, v166, v165 quad_perm:[1,0,3,2] row_mask:0xf bank_mask:0xf bound_ctrl:1
	v_cndmask_b32_e64 v167, v161, v165, s[32:33]
	v_cndmask_b32_e64 v163, v165, v161, s[32:33]
	s_nop 1
	v_add_f32_dpp v163, v167, v163 quad_perm:[2,3,0,1] row_mask:0xf bank_mask:0xf bound_ctrl:1
	v_cvt_f16_f32_e32 v163, v163
	ds_write_b16 v14, v163 offset:2176
	s_waitcnt vmcnt(16)
	v_add_f32_e32 v176, v176, v177
	v_add_f32_e32 v178, v178, v179
	v_add_f32_e32 v180, v180, v181
	v_add_f32_e32 v182, v182, v183
	v_add_f32_e32 v184, v184, v185
	v_add_f32_e32 v186, v186, v187
	v_add_f32_e32 v188, v188, v189
	v_add_f32_e32 v190, v190, v191
	v_add_f32_e32 v176, v176, v178
	v_add_f32_e32 v180, v180, v182
	v_add_f32_e32 v184, v184, v186
	v_add_f32_e32 v188, v188, v190
	v_cndmask_b32_e64 v178, v176, v180, s[30:31]
	v_cndmask_b32_e64 v182, v184, v188, s[30:31]
	v_cndmask_b32_e64 v177, v180, v176, s[30:31]
	v_cndmask_b32_e64 v181, v188, v184, s[30:31]
	v_add_f32_dpp v177, v178, v177 quad_perm:[1,0,3,2] row_mask:0xf bank_mask:0xf bound_ctrl:1
	v_add_f32_dpp v181, v182, v181 quad_perm:[1,0,3,2] row_mask:0xf bank_mask:0xf bound_ctrl:1
	v_cndmask_b32_e64 v183, v177, v181, s[32:33]
	v_cndmask_b32_e64 v179, v181, v177, s[32:33]
	s_nop 1
	v_add_f32_dpp v179, v183, v179 quad_perm:[2,3,0,1] row_mask:0xf bank_mask:0xf bound_ctrl:1
	v_cvt_f16_f32_e32 v179, v179
	ds_write_b16 v14, v179 offset:3264
	s_waitcnt vmcnt(12)
	v_add_f32_e32 v192, v192, v193
	v_add_f32_e32 v194, v194, v195
	v_add_f32_e32 v196, v196, v197
	v_add_f32_e32 v198, v198, v199
	v_add_f32_e32 v200, v200, v201
	v_add_f32_e32 v202, v202, v203
	v_add_f32_e32 v204, v204, v205
	v_add_f32_e32 v206, v206, v207
	v_add_f32_e32 v192, v192, v194
	v_add_f32_e32 v196, v196, v198
	v_add_f32_e32 v200, v200, v202
	v_add_f32_e32 v204, v204, v206
	v_cndmask_b32_e64 v194, v192, v196, s[30:31]
	v_cndmask_b32_e64 v198, v200, v204, s[30:31]
	v_cndmask_b32_e64 v193, v196, v192, s[30:31]
	v_cndmask_b32_e64 v197, v204, v200, s[30:31]
	v_add_f32_dpp v193, v194, v193 quad_perm:[1,0,3,2] row_mask:0xf bank_mask:0xf bound_ctrl:1
	v_add_f32_dpp v197, v198, v197 quad_perm:[1,0,3,2] row_mask:0xf bank_mask:0xf bound_ctrl:1
	v_cndmask_b32_e64 v199, v193, v197, s[32:33]
	v_cndmask_b32_e64 v195, v197, v193, s[32:33]
	s_nop 1
	v_add_f32_dpp v195, v199, v195 quad_perm:[2,3,0,1] row_mask:0xf bank_mask:0xf bound_ctrl:1
	v_cvt_f16_f32_e32 v195, v195
	ds_write_b16 v14, v195 offset:4352
	s_waitcnt vmcnt(8)
	v_add_f32_e32 v208, v208, v209
	v_add_f32_e32 v210, v210, v211
	v_add_f32_e32 v212, v212, v213
	v_add_f32_e32 v214, v214, v215
	v_add_f32_e32 v216, v216, v217
	v_add_f32_e32 v218, v218, v219
	v_add_f32_e32 v220, v220, v221
	v_add_f32_e32 v222, v222, v223
	v_add_f32_e32 v208, v208, v210
	v_add_f32_e32 v212, v212, v214
	v_add_f32_e32 v216, v216, v218
	v_add_f32_e32 v220, v220, v222
	v_cndmask_b32_e64 v210, v208, v212, s[30:31]
	v_cndmask_b32_e64 v214, v216, v220, s[30:31]
	v_cndmask_b32_e64 v209, v212, v208, s[30:31]
	v_cndmask_b32_e64 v213, v220, v216, s[30:31]
	v_add_f32_dpp v209, v210, v209 quad_perm:[1,0,3,2] row_mask:0xf bank_mask:0xf bound_ctrl:1
	v_add_f32_dpp v213, v214, v213 quad_perm:[1,0,3,2] row_mask:0xf bank_mask:0xf bound_ctrl:1
	v_cndmask_b32_e64 v215, v209, v213, s[32:33]
	v_cndmask_b32_e64 v211, v213, v209, s[32:33]
	s_nop 1
	v_add_f32_dpp v211, v215, v211 quad_perm:[2,3,0,1] row_mask:0xf bank_mask:0xf bound_ctrl:1
	v_cvt_f16_f32_e32 v211, v211
	ds_write_b16 v14, v211 offset:5440
	s_waitcnt vmcnt(4)
	v_add_f32_e32 v224, v224, v225
	v_add_f32_e32 v226, v226, v227
	v_add_f32_e32 v228, v228, v229
	v_add_f32_e32 v230, v230, v231
	v_add_f32_e32 v232, v232, v233
	v_add_f32_e32 v234, v234, v235
	v_add_f32_e32 v236, v236, v237
	v_add_f32_e32 v238, v238, v239
	v_add_f32_e32 v224, v224, v226
	v_add_f32_e32 v228, v228, v230
	v_add_f32_e32 v232, v232, v234
	v_add_f32_e32 v236, v236, v238
	v_cndmask_b32_e64 v226, v224, v228, s[30:31]
	v_cndmask_b32_e64 v230, v232, v236, s[30:31]
	v_cndmask_b32_e64 v225, v228, v224, s[30:31]
	v_cndmask_b32_e64 v229, v236, v232, s[30:31]
	v_add_f32_dpp v225, v226, v225 quad_perm:[1,0,3,2] row_mask:0xf bank_mask:0xf bound_ctrl:1
	v_add_f32_dpp v229, v230, v229 quad_perm:[1,0,3,2] row_mask:0xf bank_mask:0xf bound_ctrl:1
	v_cndmask_b32_e64 v231, v225, v229, s[32:33]
	v_cndmask_b32_e64 v227, v229, v225, s[32:33]
	s_nop 1
	v_add_f32_dpp v227, v231, v227 quad_perm:[2,3,0,1] row_mask:0xf bank_mask:0xf bound_ctrl:1
	v_cvt_f16_f32_e32 v227, v227
	ds_write_b16 v14, v227 offset:6528
	s_waitcnt vmcnt(0)
	v_add_f32_e32 v240, v240, v241
	v_add_f32_e32 v242, v242, v243
	v_add_f32_e32 v244, v244, v245
	v_add_f32_e32 v246, v246, v247
	v_add_f32_e32 v248, v248, v249
	v_add_f32_e32 v250, v250, v251
	v_add_f32_e32 v252, v252, v253
	v_add_f32_e32 v254, v254, v255
	v_add_f32_e32 v240, v240, v242
	v_add_f32_e32 v244, v244, v246
	v_add_f32_e32 v248, v248, v250
	v_add_f32_e32 v252, v252, v254
	v_cndmask_b32_e64 v242, v240, v244, s[30:31]
	v_cndmask_b32_e64 v246, v248, v252, s[30:31]
	v_cndmask_b32_e64 v241, v244, v240, s[30:31]
	v_cndmask_b32_e64 v245, v252, v248, s[30:31]
	v_add_f32_dpp v241, v242, v241 quad_perm:[1,0,3,2] row_mask:0xf bank_mask:0xf bound_ctrl:1
	v_add_f32_dpp v245, v246, v245 quad_perm:[1,0,3,2] row_mask:0xf bank_mask:0xf bound_ctrl:1
	v_cndmask_b32_e64 v247, v241, v245, s[32:33]
	v_cndmask_b32_e64 v243, v245, v241, s[32:33]
	s_nop 1
	v_add_f32_dpp v243, v247, v243 quad_perm:[2,3,0,1] row_mask:0xf bank_mask:0xf bound_ctrl:1
	v_cvt_f16_f32_e32 v243, v243
	ds_write_b16 v14, v243 offset:7616
	s_waitcnt lgkmcnt(0)
	s_barrier
	ds_read_b128 v[160:163], v15 offset:0
	ds_read_b128 v[164:167], v15 offset:32
	ds_read_b128 v[168:171], v15 offset:64
	ds_read_b128 v[172:175], v15 offset:96
	ds_read_b128 v[176:179], v15 offset:128
	ds_read_b128 v[180:183], v15 offset:160
	ds_read_b128 v[184:187], v15 offset:192
	ds_read_b128 v[188:191], v15 offset:224
	s_waitcnt lgkmcnt(7)
	v_mfma_f32_32x32x16_f16 v[128:143], v[160:163], v[32:35], 0
	v_mfma_f32_32x32x16_f16 v[144:159], v[160:163], v[64:67], 0
	s_waitcnt lgkmcnt(6)
	v_mfma_f32_32x32x16_f16 v[128:143], v[164:167], v[36:39], v[128:143]
	v_mfma_f32_32x32x16_f16 v[144:159], v[164:167], v[68:71], v[144:159]
	s_waitcnt lgkmcnt(5)
	v_mfma_f32_32x32x16_f16 v[128:143], v[168:171], v[40:43], v[128:143]
	v_mfma_f32_32x32x16_f16 v[144:159], v[168:171], v[72:75], v[144:159]
	s_waitcnt lgkmcnt(4)
	v_mfma_f32_32x32x16_f16 v[128:143], v[172:175], v[44:47], v[128:143]
	v_mfma_f32_32x32x16_f16 v[144:159], v[172:175], v[76:79], v[144:159]
	s_waitcnt lgkmcnt(3)
	v_mfma_f32_32x32x16_f16 v[128:143], v[176:179], v[48:51], v[128:143]
	v_mfma_f32_32x32x16_f16 v[144:159], v[176:179], v[80:83], v[144:159]
	s_waitcnt lgkmcnt(2)
	v_mfma_f32_32x32x16_f16 v[128:143], v[180:183], v[52:55], v[128:143]
	v_mfma_f32_32x32x16_f16 v[144:159], v[180:183], v[84:87], v[144:159]
	s_waitcnt lgkmcnt(1)
	v_mfma_f32_32x32x16_f16 v[128:143], v[184:187], v[56:59], v[128:143]
	v_mfma_f32_32x32x16_f16 v[144:159], v[184:187], v[88:91], v[144:159]
	s_waitcnt lgkmcnt(0)
	v_mfma_f32_32x32x16_f16 v[128:143], v[188:191], v[60:63], v[128:143]
	v_mfma_f32_32x32x16_f16 v[144:159], v[188:191], v[92:95], v[144:159]
	s_nop 15
	s_nop 3
	v_mul_f32_e32 v16, v96, v128
	v_mul_f32_e32 v17, v97, v129
	v_mul_f32_e32 v18, v98, v130
	v_mul_f32_e32 v19, v99, v131
	v_fma_f32 v16, -v112, v144, v16
	v_fma_f32 v17, -v113, v145, v17
	v_fma_f32 v18, -v114, v146, v18
	v_fma_f32 v19, -v115, v147, v19
	v_fma_f32 v16, v100, v132, v16
	v_fma_f32 v16, -v116, v148, v16
	v_fma_f32 v17, v101, v133, v17
	v_fma_f32 v17, -v117, v149, v17
	v_fma_f32 v18, v102, v134, v18
	v_fma_f32 v18, -v118, v150, v18
	v_fma_f32 v19, v103, v135, v19
	v_fma_f32 v19, -v119, v151, v19
	v_fma_f32 v16, v104, v136, v16
	v_fma_f32 v16, -v120, v152, v16
	v_fma_f32 v17, v105, v137, v17
	v_fma_f32 v17, -v121, v153, v17
	v_fma_f32 v18, v106, v138, v18
	v_fma_f32 v18, -v122, v154, v18
	v_fma_f32 v19, v107, v139, v19
	v_fma_f32 v19, -v123, v155, v19
	v_fma_f32 v16, v108, v140, v16
	v_fma_f32 v16, -v124, v156, v16
	v_fma_f32 v17, v109, v141, v17
	v_fma_f32 v17, -v125, v157, v17
	v_fma_f32 v18, v110, v142, v18
	v_fma_f32 v18, -v126, v158, v18
	v_fma_f32 v19, v111, v143, v19
	v_fma_f32 v19, -v127, v159, v19
	v_add_f32_e32 v16, v16, v17
	v_add_f32_e32 v18, v18, v19
	v_add_f32_e32 v16, v16, v18
	v_mov_b32_e32 v17, v16
	s_lshl_b32 s6, s6, 6
	s_add_i32 s6, s6, s7
	s_lshl_b32 s6, s6, 10
	v_permlane32_swap_b32_e32 v16, v17
	v_add_u32_e32 v5, s6, v5
	v_cmp_gt_u32_e32 vcc, 32, v1
	v_add_f32_e32 v16, v16, v17
	s_and_saveexec_b64 s[2:3], vcc
	s_cbranch_execz .Ldog_main_done
	global_store_dword v5, v16, s[26:27]
